# adds: P10 unit-top dead clear moved off hot path; P0 adaLN GEMV k-loop double-buffered (next trip's loads issued before current FMAs)
# speedup vs baseline: 1.0335x; 1.0006x over previous
; __device__ __forceinline__ void phase0(const Args& a, LAS unsigned char* lds, int tid, int lane, int wave, int vcu, int G, bool do_mod = true, bool do_tr = true) {
;     ...
;         for (int chunk = vcu; chunk < 192; chunk += G) {
;             const int n0 = chunk * 64, ks = lane >> 4, n4 = (lane & 15) * 4;
;             f32x4 acc[9];
; #pragma unroll
;             for (int r = 0; r < 9; ++r) acc[r] = (f32x4){0.f, 0.f, 0.f, 0.f};
; #pragma unroll 4
;             for (int kk = 0; kk < 256; kk += 4) { const int k = wave * 256 + kk + ks; const f32x4 wv = __builtin_nontemporal_load((const f32x4*)(wm + (size_t)k * 12288 + n0 + n4));
; #pragma unroll
;                 for (int r = 0; r < 9; ++r) { const float s = sc[r * 2048 + k]; acc[r] += wv * s; } }
.LBB0_12:
	s_lshl_b32 s4, s13, 6
	s_ashr_i32 s5, s4, 31
	v_lshl_add_u64 v[34:35], s[4:5], 2, v[4:5]
	s_mov_b32 s2, -4
	v_mov_b32_e32 v48, v82
	v_mov_b32_e32 v42, 0
	v_mov_b32_e32 v43, v3
	v_mov_b32_e32 v40, 0
	v_mov_b32_e32 v41, v3
	v_mov_b32_e32 v38, 0
	v_mov_b32_e32 v39, v3
	v_mov_b32_e32 v36, 0
	v_mov_b32_e32 v37, v3
	v_mov_b32_e32 v32, 0
	v_mov_b32_e32 v33, v3
	v_mov_b32_e32 v30, 0
	v_mov_b32_e32 v31, v3
	v_mov_b32_e32 v28, 0
	v_mov_b32_e32 v29, v3
	v_mov_b32_e32 v26, 0
	v_mov_b32_e32 v27, v3
	v_mov_b32_e32 v24, 0
	v_mov_b32_e32 v25, v3
	v_mov_b32_e32 v22, 0
	v_mov_b32_e32 v23, v3
	v_mov_b32_e32 v20, 0
	v_mov_b32_e32 v21, v3
	v_mov_b32_e32 v18, 0
	v_mov_b32_e32 v19, v3
	v_mov_b32_e32 v16, 0
	v_mov_b32_e32 v17, v3
	v_mov_b32_e32 v14, 0
	v_mov_b32_e32 v15, v3
	v_mov_b32_e32 v10, 0
	v_mov_b32_e32 v11, v3
	v_mov_b32_e32 v6, 0
	v_mov_b32_e32 v7, v3
	v_mov_b32_e32 v12, 0
	v_mov_b32_e32 v13, v3
	v_mov_b32_e32 v8, 0
	v_mov_b32_e32 v9, v3
	v_add_u32_e32 v162, 0x2000, v48
	v_add_u32_e32 v163, 0x4000, v48
	v_add_u32_e32 v164, 0x6000, v48
	v_add_u32_e32 v165, 0x8000, v48
	v_add_u32_e32 v166, 0xa000, v48
	v_add_u32_e32 v167, 0xc000, v48
	v_add_u32_e32 v168, 0xe000, v48
	v_add_u32_e32 v169, 0x10000, v48
	v_add_u32_e32 v156, s2, v81
	v_add_u32_e32 v157, 4, v156
	v_min_u32_e32 v157, 0x7ff, v157
	v_add_u32_e32 v158, 8, v156
	v_min_u32_e32 v158, 0x7ff, v158
	v_add_u32_e32 v159, 12, v156
	v_min_u32_e32 v159, 0x7ff, v159
	v_add_u32_e32 v160, 16, v156
	v_min_u32_e32 v160, 0x7ff, v160
	v_mad_i64_i32 v[50:51], s[8:9], v157, s11, v[34:35]
	v_mad_i64_i32 v[54:55], s[8:9], v158, s11, v[34:35]
	v_mad_i64_i32 v[58:59], s[8:9], v159, s11, v[34:35]
	v_mad_i64_i32 v[62:63], s[8:9], v160, s11, v[34:35]
	global_load_dwordx4 v[50:53], v[50:51], off nt
	global_load_dwordx4 v[54:57], v[54:55], off nt
	global_load_dwordx4 v[58:61], v[58:59], off nt
	global_load_dwordx4 v[62:65], v[62:63], off nt
.LBB0_13:
	v_add_u32_e32 v156, s2, v81
	v_add_u32_e32 v157, 20, v156
	v_min_u32_e32 v157, 0x7ff, v157
	v_add_u32_e32 v158, 24, v156
	v_min_u32_e32 v158, 0x7ff, v158
	v_add_u32_e32 v159, 28, v156
	v_min_u32_e32 v159, 0x7ff, v159
	v_add_u32_e32 v160, 32, v156
	v_min_u32_e32 v160, 0x7ff, v160
	v_mad_i64_i32 v[140:141], s[8:9], v157, s11, v[34:35]
	v_mad_i64_i32 v[144:145], s[8:9], v158, s11, v[34:35]
	v_mad_i64_i32 v[148:149], s[8:9], v159, s11, v[34:35]
	v_mad_i64_i32 v[152:153], s[8:9], v160, s11, v[34:35]
	global_load_dwordx4 v[140:143], v[140:141], off nt
	global_load_dwordx4 v[144:147], v[144:145], off nt
	global_load_dwordx4 v[148:151], v[148:149], off nt
	global_load_dwordx4 v[152:155], v[152:153], off nt
	ds_read2_b32 v[44:45], v48 offset1:4
	ds_read2_b32 v[46:47], v48 offset0:8 offset1:12
	ds_read2_b32 v[66:67], v162 offset1:4
	ds_read2_b32 v[90:91], v162 offset0:8 offset1:12
	ds_read2_b32 v[68:69], v163 offset1:4
	ds_read2_b32 v[92:93], v163 offset0:8 offset1:12
	ds_read2_b32 v[70:71], v164 offset1:4
	ds_read2_b32 v[94:95], v164 offset0:8 offset1:12
	ds_read2_b32 v[74:75], v165 offset1:4
	ds_read2_b32 v[96:97], v165 offset0:8 offset1:12
	ds_read2_b32 v[76:77], v166 offset1:4
	ds_read2_b32 v[100:101], v166 offset0:8 offset1:12
	ds_read2_b32 v[84:85], v167 offset1:4
	ds_read2_b32 v[102:103], v167 offset0:8 offset1:12
	ds_read2_b32 v[86:87], v168 offset1:4
	ds_read2_b32 v[104:105], v168 offset0:8 offset1:12
	ds_read_b32 v72, v169
	ds_read_b32 v88, v169 offset:16
	ds_read_b32 v98, v169 offset:32
	ds_read_b32 v106, v169 offset:48
	s_waitcnt lgkmcnt(0)
	s_waitcnt vmcnt(7)
	v_pk_fma_f32 v[42:43], v[50:51], v[44:45], v[42:43] op_sel_hi:[1,0,1]
	v_pk_fma_f32 v[40:41], v[52:53], v[44:45], v[40:41] op_sel_hi:[1,0,1]
	v_pk_fma_f32 v[38:39], v[50:51], v[66:67], v[38:39] op_sel_hi:[1,0,1]
	v_pk_fma_f32 v[36:37], v[52:53], v[66:67], v[36:37] op_sel_hi:[1,0,1]
	v_pk_fma_f32 v[32:33], v[50:51], v[68:69], v[32:33] op_sel_hi:[1,0,1]
	v_pk_fma_f32 v[30:31], v[52:53], v[68:69], v[30:31] op_sel_hi:[1,0,1]
	v_pk_fma_f32 v[28:29], v[50:51], v[70:71], v[28:29] op_sel_hi:[1,0,1]
	v_pk_fma_f32 v[26:27], v[52:53], v[70:71], v[26:27] op_sel_hi:[1,0,1]
	v_pk_fma_f32 v[24:25], v[50:51], v[74:75], v[24:25] op_sel_hi:[1,0,1]
	v_pk_fma_f32 v[22:23], v[52:53], v[74:75], v[22:23] op_sel_hi:[1,0,1]
	v_pk_fma_f32 v[20:21], v[50:51], v[76:77], v[20:21] op_sel_hi:[1,0,1]
	v_pk_fma_f32 v[18:19], v[52:53], v[76:77], v[18:19] op_sel_hi:[1,0,1]
	v_pk_fma_f32 v[16:17], v[50:51], v[84:85], v[16:17] op_sel_hi:[1,0,1]
	v_pk_fma_f32 v[14:15], v[52:53], v[84:85], v[14:15] op_sel_hi:[1,0,1]
	v_pk_fma_f32 v[10:11], v[50:51], v[86:87], v[10:11] op_sel_hi:[1,0,1]
	v_pk_fma_f32 v[6:7], v[52:53], v[86:87], v[6:7] op_sel_hi:[1,0,1]
	v_pk_fma_f32 v[12:13], v[50:51], v[72:73], v[12:13] op_sel_hi:[1,0,1]
	v_pk_fma_f32 v[8:9], v[52:53], v[72:73], v[8:9] op_sel_hi:[1,0,1]
	s_waitcnt vmcnt(6)
	v_pk_fma_f32 v[42:43], v[54:55], v[44:45], v[42:43] op_sel:[0,1,0] op_sel_hi:[1,1,1]
	v_pk_fma_f32 v[40:41], v[56:57], v[44:45], v[40:41] op_sel:[0,1,0] op_sel_hi:[1,1,1]
	v_pk_fma_f32 v[38:39], v[54:55], v[66:67], v[38:39] op_sel:[0,1,0] op_sel_hi:[1,1,1]
	v_pk_fma_f32 v[36:37], v[56:57], v[66:67], v[36:37] op_sel:[0,1,0] op_sel_hi:[1,1,1]
	v_pk_fma_f32 v[32:33], v[54:55], v[68:69], v[32:33] op_sel:[0,1,0] op_sel_hi:[1,1,1]
	v_pk_fma_f32 v[30:31], v[56:57], v[68:69], v[30:31] op_sel:[0,1,0] op_sel_hi:[1,1,1]
	v_pk_fma_f32 v[28:29], v[54:55], v[70:71], v[28:29] op_sel:[0,1,0] op_sel_hi:[1,1,1]
	v_pk_fma_f32 v[26:27], v[56:57], v[70:71], v[26:27] op_sel:[0,1,0] op_sel_hi:[1,1,1]
	v_pk_fma_f32 v[24:25], v[54:55], v[74:75], v[24:25] op_sel:[0,1,0] op_sel_hi:[1,1,1]
	v_pk_fma_f32 v[22:23], v[56:57], v[74:75], v[22:23] op_sel:[0,1,0] op_sel_hi:[1,1,1]
	v_pk_fma_f32 v[20:21], v[54:55], v[76:77], v[20:21] op_sel:[0,1,0] op_sel_hi:[1,1,1]
	v_pk_fma_f32 v[18:19], v[56:57], v[76:77], v[18:19] op_sel:[0,1,0] op_sel_hi:[1,1,1]
	v_pk_fma_f32 v[16:17], v[54:55], v[84:85], v[16:17] op_sel:[0,1,0] op_sel_hi:[1,1,1]
	v_pk_fma_f32 v[14:15], v[56:57], v[84:85], v[14:15] op_sel:[0,1,0] op_sel_hi:[1,1,1]
	v_pk_fma_f32 v[10:11], v[54:55], v[86:87], v[10:11] op_sel:[0,1,0] op_sel_hi:[1,1,1]
	v_pk_fma_f32 v[6:7], v[56:57], v[86:87], v[6:7] op_sel:[0,1,0] op_sel_hi:[1,1,1]
	v_pk_fma_f32 v[12:13], v[54:55], v[88:89], v[12:13] op_sel_hi:[1,0,1]
	v_pk_fma_f32 v[8:9], v[56:57], v[88:89], v[8:9] op_sel_hi:[1,0,1]
	s_waitcnt vmcnt(5)
; __device__ __forceinline__ void phase0(const Args& a, LAS unsigned char* lds, int tid, int lane, int wave, int vcu, int G, bool do_mod = true, bool do_tr = true) {
;     ...
;             for (int r = 0; r < 9; ++r) acc[r] = (f32x4){0.f, 0.f, 0.f, 0.f};
; #pragma unroll 4
;             for (int kk = 0; kk < 256; kk += 4) { const int k = wave * 256 + kk + ks; const f32x4 wv = __builtin_nontemporal_load((const f32x4*)(wm + (size_t)k * 12288 + n0 + n4));
; #pragma unroll
;                 for (int r = 0; r < 9; ++r) { const float s = sc[r * 2048 + k]; acc[r] += wv * s; } }
	v_pk_fma_f32 v[42:43], v[58:59], v[46:47], v[42:43] op_sel_hi:[1,0,1]
	v_pk_fma_f32 v[40:41], v[60:61], v[46:47], v[40:41] op_sel_hi:[1,0,1]
	v_pk_fma_f32 v[38:39], v[58:59], v[90:91], v[38:39] op_sel_hi:[1,0,1]
	v_pk_fma_f32 v[36:37], v[60:61], v[90:91], v[36:37] op_sel_hi:[1,0,1]
	v_pk_fma_f32 v[32:33], v[58:59], v[92:93], v[32:33] op_sel_hi:[1,0,1]
	v_pk_fma_f32 v[30:31], v[60:61], v[92:93], v[30:31] op_sel_hi:[1,0,1]
	v_pk_fma_f32 v[28:29], v[58:59], v[94:95], v[28:29] op_sel_hi:[1,0,1]
	v_pk_fma_f32 v[26:27], v[60:61], v[94:95], v[26:27] op_sel_hi:[1,0,1]
	v_pk_fma_f32 v[24:25], v[58:59], v[96:97], v[24:25] op_sel_hi:[1,0,1]
	v_pk_fma_f32 v[22:23], v[60:61], v[96:97], v[22:23] op_sel_hi:[1,0,1]
	v_pk_fma_f32 v[20:21], v[58:59], v[100:101], v[20:21] op_sel_hi:[1,0,1]
	v_pk_fma_f32 v[18:19], v[60:61], v[100:101], v[18:19] op_sel_hi:[1,0,1]
	v_pk_fma_f32 v[16:17], v[58:59], v[102:103], v[16:17] op_sel_hi:[1,0,1]
	v_pk_fma_f32 v[14:15], v[60:61], v[102:103], v[14:15] op_sel_hi:[1,0,1]
	v_pk_fma_f32 v[10:11], v[58:59], v[104:105], v[10:11] op_sel_hi:[1,0,1]
	v_pk_fma_f32 v[6:7], v[60:61], v[104:105], v[6:7] op_sel_hi:[1,0,1]
	v_pk_fma_f32 v[12:13], v[58:59], v[98:99], v[12:13] op_sel_hi:[1,0,1]
	v_pk_fma_f32 v[8:9], v[60:61], v[98:99], v[8:9] op_sel_hi:[1,0,1]
	s_waitcnt vmcnt(4)
	v_pk_fma_f32 v[42:43], v[62:63], v[46:47], v[42:43] op_sel:[0,1,0] op_sel_hi:[1,1,1]
	v_pk_fma_f32 v[40:41], v[64:65], v[46:47], v[40:41] op_sel:[0,1,0] op_sel_hi:[1,1,1]
	v_pk_fma_f32 v[38:39], v[62:63], v[90:91], v[38:39] op_sel:[0,1,0] op_sel_hi:[1,1,1]
	v_pk_fma_f32 v[36:37], v[64:65], v[90:91], v[36:37] op_sel:[0,1,0] op_sel_hi:[1,1,1]
	v_pk_fma_f32 v[32:33], v[62:63], v[92:93], v[32:33] op_sel:[0,1,0] op_sel_hi:[1,1,1]
	v_pk_fma_f32 v[30:31], v[64:65], v[92:93], v[30:31] op_sel:[0,1,0] op_sel_hi:[1,1,1]
	v_pk_fma_f32 v[28:29], v[62:63], v[94:95], v[28:29] op_sel:[0,1,0] op_sel_hi:[1,1,1]
	v_pk_fma_f32 v[26:27], v[64:65], v[94:95], v[26:27] op_sel:[0,1,0] op_sel_hi:[1,1,1]
	v_pk_fma_f32 v[24:25], v[62:63], v[96:97], v[24:25] op_sel:[0,1,0] op_sel_hi:[1,1,1]
	v_pk_fma_f32 v[22:23], v[64:65], v[96:97], v[22:23] op_sel:[0,1,0] op_sel_hi:[1,1,1]
	v_pk_fma_f32 v[20:21], v[62:63], v[100:101], v[20:21] op_sel:[0,1,0] op_sel_hi:[1,1,1]
	v_pk_fma_f32 v[18:19], v[64:65], v[100:101], v[18:19] op_sel:[0,1,0] op_sel_hi:[1,1,1]
	v_pk_fma_f32 v[16:17], v[62:63], v[102:103], v[16:17] op_sel:[0,1,0] op_sel_hi:[1,1,1]
	v_pk_fma_f32 v[14:15], v[64:65], v[102:103], v[14:15] op_sel:[0,1,0] op_sel_hi:[1,1,1]
	v_pk_fma_f32 v[10:11], v[62:63], v[104:105], v[10:11] op_sel:[0,1,0] op_sel_hi:[1,1,1]
	v_pk_fma_f32 v[6:7], v[64:65], v[104:105], v[6:7] op_sel:[0,1,0] op_sel_hi:[1,1,1]
	v_pk_fma_f32 v[12:13], v[62:63], v[106:107], v[12:13] op_sel_hi:[1,0,1]
	v_pk_fma_f32 v[8:9], v[64:65], v[106:107], v[8:9] op_sel_hi:[1,0,1]
	s_add_i32 s2, s2, 16
	v_add_u32_e32 v48, 64, v48
	v_add_u32_e32 v162, 64, v162
	v_add_u32_e32 v163, 64, v163
	v_add_u32_e32 v164, 64, v164
	v_add_u32_e32 v165, 64, v165
	v_add_u32_e32 v166, 64, v166
	v_add_u32_e32 v167, 64, v167
	v_add_u32_e32 v168, 64, v168
	v_add_u32_e32 v169, 64, v169
	v_add_u32_e32 v156, s2, v81
	v_add_u32_e32 v157, 20, v156
	v_min_u32_e32 v157, 0x7ff, v157
	v_add_u32_e32 v158, 24, v156
	v_min_u32_e32 v158, 0x7ff, v158
	v_add_u32_e32 v159, 28, v156
	v_min_u32_e32 v159, 0x7ff, v159
	v_add_u32_e32 v160, 32, v156
	v_min_u32_e32 v160, 0x7ff, v160
	v_mad_i64_i32 v[50:51], s[8:9], v157, s11, v[34:35]
	v_mad_i64_i32 v[54:55], s[8:9], v158, s11, v[34:35]
	v_mad_i64_i32 v[58:59], s[8:9], v159, s11, v[34:35]
	v_mad_i64_i32 v[62:63], s[8:9], v160, s11, v[34:35]
	global_load_dwordx4 v[50:53], v[50:51], off nt
	global_load_dwordx4 v[54:57], v[54:55], off nt
	global_load_dwordx4 v[58:61], v[58:59], off nt
	global_load_dwordx4 v[62:65], v[62:63], off nt
	ds_read2_b32 v[44:45], v48 offset1:4
	ds_read2_b32 v[46:47], v48 offset0:8 offset1:12
	ds_read2_b32 v[66:67], v162 offset1:4
	ds_read2_b32 v[90:91], v162 offset0:8 offset1:12
	ds_read2_b32 v[68:69], v163 offset1:4
	ds_read2_b32 v[92:93], v163 offset0:8 offset1:12
	ds_read2_b32 v[70:71], v164 offset1:4
	ds_read2_b32 v[94:95], v164 offset0:8 offset1:12
	ds_read2_b32 v[74:75], v165 offset1:4
	ds_read2_b32 v[96:97], v165 offset0:8 offset1:12
	ds_read2_b32 v[76:77], v166 offset1:4
	ds_read2_b32 v[100:101], v166 offset0:8 offset1:12
	ds_read2_b32 v[84:85], v167 offset1:4
	ds_read2_b32 v[102:103], v167 offset0:8 offset1:12
	ds_read2_b32 v[86:87], v168 offset1:4
	ds_read2_b32 v[104:105], v168 offset0:8 offset1:12
	ds_read_b32 v72, v169
	ds_read_b32 v88, v169 offset:16
	ds_read_b32 v98, v169 offset:32
	ds_read_b32 v106, v169 offset:48
	s_waitcnt lgkmcnt(0)
	s_waitcnt vmcnt(7)
	v_pk_fma_f32 v[42:43], v[140:141], v[44:45], v[42:43] op_sel_hi:[1,0,1]
	v_pk_fma_f32 v[40:41], v[142:143], v[44:45], v[40:41] op_sel_hi:[1,0,1]
	v_pk_fma_f32 v[38:39], v[140:141], v[66:67], v[38:39] op_sel_hi:[1,0,1]
	v_pk_fma_f32 v[36:37], v[142:143], v[66:67], v[36:37] op_sel_hi:[1,0,1]
	v_pk_fma_f32 v[32:33], v[140:141], v[68:69], v[32:33] op_sel_hi:[1,0,1]
	v_pk_fma_f32 v[30:31], v[142:143], v[68:69], v[30:31] op_sel_hi:[1,0,1]
	v_pk_fma_f32 v[28:29], v[140:141], v[70:71], v[28:29] op_sel_hi:[1,0,1]
	v_pk_fma_f32 v[26:27], v[142:143], v[70:71], v[26:27] op_sel_hi:[1,0,1]
	v_pk_fma_f32 v[24:25], v[140:141], v[74:75], v[24:25] op_sel_hi:[1,0,1]
	v_pk_fma_f32 v[22:23], v[142:143], v[74:75], v[22:23] op_sel_hi:[1,0,1]
	v_pk_fma_f32 v[20:21], v[140:141], v[76:77], v[20:21] op_sel_hi:[1,0,1]
	v_pk_fma_f32 v[18:19], v[142:143], v[76:77], v[18:19] op_sel_hi:[1,0,1]
	v_pk_fma_f32 v[16:17], v[140:141], v[84:85], v[16:17] op_sel_hi:[1,0,1]
	v_pk_fma_f32 v[14:15], v[142:143], v[84:85], v[14:15] op_sel_hi:[1,0,1]
	v_pk_fma_f32 v[10:11], v[140:141], v[86:87], v[10:11] op_sel_hi:[1,0,1]
	v_pk_fma_f32 v[6:7], v[142:143], v[86:87], v[6:7] op_sel_hi:[1,0,1]
	v_pk_fma_f32 v[12:13], v[140:141], v[72:73], v[12:13] op_sel_hi:[1,0,1]
	v_pk_fma_f32 v[8:9], v[142:143], v[72:73], v[8:9] op_sel_hi:[1,0,1]
	s_waitcnt vmcnt(6)
; __device__ __forceinline__ void phase0(const Args& a, LAS unsigned char* lds, int tid, int lane, int wave, int vcu, int G, bool do_mod = true, bool do_tr = true) {
;     ...
;             for (int r = 0; r < 9; ++r) acc[r] = (f32x4){0.f, 0.f, 0.f, 0.f};
; #pragma unroll 4
;             for (int kk = 0; kk < 256; kk += 4) { const int k = wave * 256 + kk + ks; const f32x4 wv = __builtin_nontemporal_load((const f32x4*)(wm + (size_t)k * 12288 + n0 + n4));
; #pragma unroll
;                 for (int r = 0; r < 9; ++r) { const float s = sc[r * 2048 + k]; acc[r] += wv * s; } }
	v_pk_fma_f32 v[42:43], v[144:145], v[44:45], v[42:43] op_sel:[0,1,0] op_sel_hi:[1,1,1]
	v_pk_fma_f32 v[40:41], v[146:147], v[44:45], v[40:41] op_sel:[0,1,0] op_sel_hi:[1,1,1]
	v_pk_fma_f32 v[38:39], v[144:145], v[66:67], v[38:39] op_sel:[0,1,0] op_sel_hi:[1,1,1]
	v_pk_fma_f32 v[36:37], v[146:147], v[66:67], v[36:37] op_sel:[0,1,0] op_sel_hi:[1,1,1]
	v_pk_fma_f32 v[32:33], v[144:145], v[68:69], v[32:33] op_sel:[0,1,0] op_sel_hi:[1,1,1]
	v_pk_fma_f32 v[30:31], v[146:147], v[68:69], v[30:31] op_sel:[0,1,0] op_sel_hi:[1,1,1]
	v_pk_fma_f32 v[28:29], v[144:145], v[70:71], v[28:29] op_sel:[0,1,0] op_sel_hi:[1,1,1]
	v_pk_fma_f32 v[26:27], v[146:147], v[70:71], v[26:27] op_sel:[0,1,0] op_sel_hi:[1,1,1]
	v_pk_fma_f32 v[24:25], v[144:145], v[74:75], v[24:25] op_sel:[0,1,0] op_sel_hi:[1,1,1]
	v_pk_fma_f32 v[22:23], v[146:147], v[74:75], v[22:23] op_sel:[0,1,0] op_sel_hi:[1,1,1]
	v_pk_fma_f32 v[20:21], v[144:145], v[76:77], v[20:21] op_sel:[0,1,0] op_sel_hi:[1,1,1]
	v_pk_fma_f32 v[18:19], v[146:147], v[76:77], v[18:19] op_sel:[0,1,0] op_sel_hi:[1,1,1]
	v_pk_fma_f32 v[16:17], v[144:145], v[84:85], v[16:17] op_sel:[0,1,0] op_sel_hi:[1,1,1]
	v_pk_fma_f32 v[14:15], v[146:147], v[84:85], v[14:15] op_sel:[0,1,0] op_sel_hi:[1,1,1]
	v_pk_fma_f32 v[10:11], v[144:145], v[86:87], v[10:11] op_sel:[0,1,0] op_sel_hi:[1,1,1]
	v_pk_fma_f32 v[6:7], v[146:147], v[86:87], v[6:7] op_sel:[0,1,0] op_sel_hi:[1,1,1]
	v_pk_fma_f32 v[12:13], v[144:145], v[88:89], v[12:13] op_sel_hi:[1,0,1]
	v_pk_fma_f32 v[8:9], v[146:147], v[88:89], v[8:9] op_sel_hi:[1,0,1]
	s_waitcnt vmcnt(5)
	v_pk_fma_f32 v[42:43], v[148:149], v[46:47], v[42:43] op_sel_hi:[1,0,1]
	v_pk_fma_f32 v[40:41], v[150:151], v[46:47], v[40:41] op_sel_hi:[1,0,1]
	v_pk_fma_f32 v[38:39], v[148:149], v[90:91], v[38:39] op_sel_hi:[1,0,1]
	v_pk_fma_f32 v[36:37], v[150:151], v[90:91], v[36:37] op_sel_hi:[1,0,1]
	v_pk_fma_f32 v[32:33], v[148:149], v[92:93], v[32:33] op_sel_hi:[1,0,1]
	v_pk_fma_f32 v[30:31], v[150:151], v[92:93], v[30:31] op_sel_hi:[1,0,1]
	v_pk_fma_f32 v[28:29], v[148:149], v[94:95], v[28:29] op_sel_hi:[1,0,1]
	v_pk_fma_f32 v[26:27], v[150:151], v[94:95], v[26:27] op_sel_hi:[1,0,1]
	v_pk_fma_f32 v[24:25], v[148:149], v[96:97], v[24:25] op_sel_hi:[1,0,1]
	v_pk_fma_f32 v[22:23], v[150:151], v[96:97], v[22:23] op_sel_hi:[1,0,1]
	v_pk_fma_f32 v[20:21], v[148:149], v[100:101], v[20:21] op_sel_hi:[1,0,1]
	v_pk_fma_f32 v[18:19], v[150:151], v[100:101], v[18:19] op_sel_hi:[1,0,1]
	v_pk_fma_f32 v[16:17], v[148:149], v[102:103], v[16:17] op_sel_hi:[1,0,1]
	v_pk_fma_f32 v[14:15], v[150:151], v[102:103], v[14:15] op_sel_hi:[1,0,1]
	v_pk_fma_f32 v[10:11], v[148:149], v[104:105], v[10:11] op_sel_hi:[1,0,1]
	v_pk_fma_f32 v[6:7], v[150:151], v[104:105], v[6:7] op_sel_hi:[1,0,1]
	v_pk_fma_f32 v[12:13], v[148:149], v[98:99], v[12:13] op_sel_hi:[1,0,1]
	v_pk_fma_f32 v[8:9], v[150:151], v[98:99], v[8:9] op_sel_hi:[1,0,1]
	s_waitcnt vmcnt(4)
	v_pk_fma_f32 v[42:43], v[152:153], v[46:47], v[42:43] op_sel:[0,1,0] op_sel_hi:[1,1,1]
	v_pk_fma_f32 v[40:41], v[154:155], v[46:47], v[40:41] op_sel:[0,1,0] op_sel_hi:[1,1,1]
	v_pk_fma_f32 v[38:39], v[152:153], v[90:91], v[38:39] op_sel:[0,1,0] op_sel_hi:[1,1,1]
	v_pk_fma_f32 v[36:37], v[154:155], v[90:91], v[36:37] op_sel:[0,1,0] op_sel_hi:[1,1,1]
	v_pk_fma_f32 v[32:33], v[152:153], v[92:93], v[32:33] op_sel:[0,1,0] op_sel_hi:[1,1,1]
	v_pk_fma_f32 v[30:31], v[154:155], v[92:93], v[30:31] op_sel:[0,1,0] op_sel_hi:[1,1,1]
	v_pk_fma_f32 v[28:29], v[152:153], v[94:95], v[28:29] op_sel:[0,1,0] op_sel_hi:[1,1,1]
	v_pk_fma_f32 v[26:27], v[154:155], v[94:95], v[26:27] op_sel:[0,1,0] op_sel_hi:[1,1,1]
	v_pk_fma_f32 v[24:25], v[152:153], v[96:97], v[24:25] op_sel:[0,1,0] op_sel_hi:[1,1,1]
	v_pk_fma_f32 v[22:23], v[154:155], v[96:97], v[22:23] op_sel:[0,1,0] op_sel_hi:[1,1,1]
	v_pk_fma_f32 v[20:21], v[152:153], v[100:101], v[20:21] op_sel:[0,1,0] op_sel_hi:[1,1,1]
	v_pk_fma_f32 v[18:19], v[154:155], v[100:101], v[18:19] op_sel:[0,1,0] op_sel_hi:[1,1,1]
	v_pk_fma_f32 v[16:17], v[152:153], v[102:103], v[16:17] op_sel:[0,1,0] op_sel_hi:[1,1,1]
	v_pk_fma_f32 v[14:15], v[154:155], v[102:103], v[14:15] op_sel:[0,1,0] op_sel_hi:[1,1,1]
	v_pk_fma_f32 v[10:11], v[152:153], v[104:105], v[10:11] op_sel:[0,1,0] op_sel_hi:[1,1,1]
	v_pk_fma_f32 v[6:7], v[154:155], v[104:105], v[6:7] op_sel:[0,1,0] op_sel_hi:[1,1,1]
	v_pk_fma_f32 v[12:13], v[152:153], v[106:107], v[12:13] op_sel_hi:[1,0,1]
	v_pk_fma_f32 v[8:9], v[154:155], v[106:107], v[8:9] op_sel_hi:[1,0,1]
	s_add_i32 s2, s2, 16
	v_add_u32_e32 v48, 64, v48
	v_add_u32_e32 v162, 64, v162
	v_add_u32_e32 v163, 64, v163
	v_add_u32_e32 v164, 64, v164
	v_add_u32_e32 v165, 64, v165
	v_add_u32_e32 v166, 64, v166
	v_add_u32_e32 v167, 64, v167
	v_add_u32_e32 v168, 64, v168
	v_add_u32_e32 v169, 64, v169
	s_cmpk_lt_u32 s2, 0xfc
	s_cbranch_scc1 .LBB0_13
; #define LAS __attribute__((address_space(3)))
; __device__ __forceinline__ void phase0(const Args& a, LAS unsigned char* lds, int tid, int lane, int wave, int vcu, int G, bool do_mod = true, bool do_tr = true) {
;     ...
; #pragma unroll
;             for (int r = 0; r < 9; ++r)
; #pragma unroll
;                 for (int j = 0; j < 4; ++j) { float v = acc[r][j]; v += __shfl_xor(v, 16); v += __shfl_xor(v, 32); acc[r][j] = v; }
;             if (lane < 16) {
; #pragma unroll
;                 for (int r = 0; r < 9; ++r) *(LAS f32x4*)(red + (wave * 9 + r) * 64 + n4) = acc[r]; }
	s_waitcnt vmcnt(0)
	ds_bpermute_b32 v34, v79, v42
	ds_bpermute_b32 v35, v79, v43
	ds_bpermute_b32 v44, v79, v40
	ds_bpermute_b32 v45, v79, v41
	ds_bpermute_b32 v46, v79, v38
	ds_bpermute_b32 v47, v79, v39
	ds_bpermute_b32 v48, v79, v36
	ds_bpermute_b32 v49, v79, v37
	ds_bpermute_b32 v50, v79, v32
	ds_bpermute_b32 v51, v79, v33
	ds_bpermute_b32 v52, v79, v30
	ds_bpermute_b32 v53, v79, v31
	ds_bpermute_b32 v54, v79, v28
	ds_bpermute_b32 v55, v79, v29
	ds_bpermute_b32 v56, v79, v26
	ds_bpermute_b32 v57, v79, v27
	ds_bpermute_b32 v58, v79, v24
	ds_bpermute_b32 v59, v79, v25
	ds_bpermute_b32 v60, v79, v22
	ds_bpermute_b32 v61, v79, v23
	ds_bpermute_b32 v62, v79, v20
	ds_bpermute_b32 v63, v79, v21
	ds_bpermute_b32 v64, v79, v18
	ds_bpermute_b32 v65, v79, v19
	ds_bpermute_b32 v66, v79, v16
	ds_bpermute_b32 v67, v79, v17
	ds_bpermute_b32 v68, v79, v14
	ds_bpermute_b32 v69, v79, v15
	ds_bpermute_b32 v70, v79, v10
	ds_bpermute_b32 v71, v79, v11
	ds_bpermute_b32 v72, v79, v6
	ds_bpermute_b32 v73, v79, v7
	ds_bpermute_b32 v74, v79, v12
	ds_bpermute_b32 v75, v79, v13
	ds_bpermute_b32 v76, v79, v8
	ds_bpermute_b32 v77, v79, v9
	s_waitcnt lgkmcnt(14)
	v_pk_add_f32 v[34:35], v[42:43], v[34:35]
	v_pk_add_f32 v[40:41], v[40:41], v[44:45]
	v_pk_add_f32 v[38:39], v[38:39], v[46:47]
	v_pk_add_f32 v[36:37], v[36:37], v[48:49]
	v_pk_add_f32 v[32:33], v[32:33], v[50:51]
	v_pk_add_f32 v[30:31], v[30:31], v[52:53]
	v_pk_add_f32 v[28:29], v[28:29], v[54:55]
	v_pk_add_f32 v[26:27], v[26:27], v[56:57]
	v_pk_add_f32 v[24:25], v[24:25], v[58:59]
	v_pk_add_f32 v[22:23], v[22:23], v[60:61]
	v_pk_add_f32 v[20:21], v[20:21], v[62:63]
	s_waitcnt lgkmcnt(12)
	v_pk_add_f32 v[18:19], v[18:19], v[64:65]
	s_waitcnt lgkmcnt(10)
	v_pk_add_f32 v[16:17], v[16:17], v[66:67]
	s_waitcnt lgkmcnt(8)
	v_pk_add_f32 v[14:15], v[14:15], v[68:69]
	s_waitcnt lgkmcnt(6)
	v_pk_add_f32 v[10:11], v[10:11], v[70:71]
	s_waitcnt lgkmcnt(4)
	v_pk_add_f32 v[6:7], v[6:7], v[72:73]
	s_waitcnt lgkmcnt(2)
	v_pk_add_f32 v[12:13], v[12:13], v[74:75]
	s_waitcnt lgkmcnt(0)
	v_pk_add_f32 v[8:9], v[8:9], v[76:77]
	ds_bpermute_b32 v42, v80, v34
	ds_bpermute_b32 v43, v80, v35
	ds_bpermute_b32 v44, v80, v40
	ds_bpermute_b32 v45, v80, v41
	ds_bpermute_b32 v46, v80, v38
	ds_bpermute_b32 v47, v80, v39
	ds_bpermute_b32 v48, v80, v36
	ds_bpermute_b32 v49, v80, v37
	ds_bpermute_b32 v50, v80, v32
	ds_bpermute_b32 v51, v80, v33
	ds_bpermute_b32 v52, v80, v30
	ds_bpermute_b32 v53, v80, v31
	ds_bpermute_b32 v54, v80, v28
	ds_bpermute_b32 v55, v80, v29
	ds_bpermute_b32 v56, v80, v26
	ds_bpermute_b32 v57, v80, v27
	ds_bpermute_b32 v58, v80, v24
	ds_bpermute_b32 v59, v80, v25
	ds_bpermute_b32 v60, v80, v22
	ds_bpermute_b32 v61, v80, v23
	ds_bpermute_b32 v62, v80, v20
	ds_bpermute_b32 v63, v80, v21
	ds_bpermute_b32 v64, v80, v18
	ds_bpermute_b32 v65, v80, v19
	ds_bpermute_b32 v66, v80, v16
	ds_bpermute_b32 v67, v80, v17
	ds_bpermute_b32 v68, v80, v14
	ds_bpermute_b32 v69, v80, v15
	ds_bpermute_b32 v70, v80, v10
	ds_bpermute_b32 v71, v80, v11
	ds_bpermute_b32 v72, v80, v6
	ds_bpermute_b32 v73, v80, v7
	ds_bpermute_b32 v74, v80, v12
	ds_bpermute_b32 v75, v80, v13
	ds_bpermute_b32 v76, v80, v8
	ds_bpermute_b32 v77, v80, v9
	s_and_saveexec_b64 s[2:3], vcc
	s_cbranch_execz .LBB0_16
	s_waitcnt lgkmcnt(0)
	v_pk_add_f32 v[76:77], v[8:9], v[76:77]
	v_pk_add_f32 v[8:9], v[6:7], v[72:73]
	v_pk_add_f32 v[6:7], v[10:11], v[70:71]
	v_pk_add_f32 v[10:11], v[16:17], v[66:67]
	v_pk_add_f32 v[16:17], v[18:19], v[64:65]
	v_pk_add_f32 v[18:19], v[24:25], v[58:59]
	v_pk_add_f32 v[24:25], v[26:27], v[56:57]
	v_pk_add_f32 v[26:27], v[32:33], v[50:51]
	v_pk_add_f32 v[32:33], v[36:37], v[48:49]
	v_pk_add_f32 v[36:37], v[40:41], v[44:45]
	v_pk_add_f32 v[34:35], v[34:35], v[42:43]
	v_pk_add_f32 v[74:75], v[12:13], v[74:75]
	v_pk_add_f32 v[12:13], v[14:15], v[68:69]
	v_pk_add_f32 v[14:15], v[20:21], v[62:63]
	v_pk_add_f32 v[20:21], v[22:23], v[60:61]
	v_pk_add_f32 v[22:23], v[28:29], v[54:55]
	v_pk_add_f32 v[28:29], v[30:31], v[52:53]
	v_pk_add_f32 v[30:31], v[38:39], v[46:47]
	ds_write_b128 v83, v[34:37]
	ds_write_b128 v83, v[30:33] offset:256
	ds_write_b128 v83, v[26:29] offset:512
	ds_write_b128 v83, v[22:25] offset:768
	ds_write_b128 v83, v[18:21] offset:1024
	ds_write_b128 v83, v[14:17] offset:1280
	ds_write_b128 v83, v[10:13] offset:1536
	ds_write_b128 v83, v[6:9] offset:1792
	ds_write_b128 v83, v[74:77] offset:2048

; #define PG8_BAR __builtin_amdgcn_s_barrier()
; template <class Epi, class Sched, bool FP8 = false>
; __device__ __forceinline__ void gemm_phase(LAS unsigned char* lds, const int K, const Sched& S, const Epi& E) {
;     ...
;         if (!has_next) break;
; #pragma unroll
;         for (int a = 0; a < 2; ++a)
; #pragma unroll
;             for (int b = 0; b < 2; ++b)
; #pragma unroll
;                 for (int m = 0; m < 4; ++m)
; #pragma unroll
;                     for (int n = 0; n < 2; ++n) acc[a][b][m][n] = (f32x4){0.f, 0.f, 0.f, 0.f};
;         cur = nxt; cA = nA; cB = nB; ++ui;
;         vA[0] = vN[0]; vA[1] = vN[1]; vA[2] = vN[2]; vA[3] = vN[3];
;         if (wr == 1) PG8_BAR;
.LBB0_1382:
	s_and_b64 vcc, exec, s[0:1]
	s_waitcnt lgkmcnt(0)
	s_cbranch_vccz .Lp10_hot
	v_mov_b32_e32 v197, 0
	v_mov_b32_e32 v196, 0
	v_mov_b32_e32 v195, 0
	v_mov_b32_e32 v194, 0
	v_mov_b32_e32 v193, 0
	v_mov_b32_e32 v192, 0
	v_mov_b32_e32 v191, 0
	v_mov_b32_e32 v190, 0
	v_mov_b32_e32 v173, 0
	v_mov_b32_e32 v172, 0
	v_mov_b32_e32 v179, 0
	v_mov_b32_e32 v178, 0
	v_mov_b32_e32 v171, 0
	v_mov_b32_e32 v170, 0
	v_mov_b32_e32 v181, 0
	v_mov_b32_e32 v180, 0
	v_mov_b32_e32 v157, 0
	v_mov_b32_e32 v156, 0
	v_mov_b32_e32 v163, 0
	v_mov_b32_e32 v162, 0
	v_mov_b32_e32 v155, 0
	v_mov_b32_e32 v154, 0
	v_mov_b32_e32 v165, 0
	v_mov_b32_e32 v164, 0
	v_mov_b32_e32 v57, 0
	v_mov_b32_e32 v56, 0
	v_mov_b32_e32 v63, 0
	v_mov_b32_e32 v62, 0
	v_mov_b32_e32 v53, 0
	v_mov_b32_e32 v52, 0
	v_mov_b32_e32 v65, 0
	v_mov_b32_e32 v64, 0
	v_mov_b32_e32 v225, 0
	v_mov_b32_e32 v224, 0
	v_mov_b32_e32 v227, 0
	v_mov_b32_e32 v226, 0
	v_mov_b32_e32 v223, 0
	v_mov_b32_e32 v222, 0
	v_mov_b32_e32 v229, 0
	v_mov_b32_e32 v228, 0
	v_mov_b32_e32 v185, 0
	v_mov_b32_e32 v184, 0
	v_mov_b32_e32 v187, 0
	v_mov_b32_e32 v186, 0
	v_mov_b32_e32 v183, 0
	v_mov_b32_e32 v182, 0
	v_mov_b32_e32 v189, 0
	v_mov_b32_e32 v188, 0
	v_mov_b32_e32 v149, 0
	v_mov_b32_e32 v148, 0
	v_mov_b32_e32 v147, 0
	v_mov_b32_e32 v146, 0
	v_mov_b32_e32 v145, 0
	v_mov_b32_e32 v144, 0
	v_mov_b32_e32 v167, 0
	v_mov_b32_e32 v166, 0
	v_mov_b32_e32 v141, 0
	v_mov_b32_e32 v140, 0
	v_mov_b32_e32 v139, 0
	v_mov_b32_e32 v138, 0
	v_mov_b32_e32 v125, 0
	v_mov_b32_e32 v124, 0
	v_mov_b32_e32 v143, 0
	v_mov_b32_e32 v142, 0
	v_mov_b32_e32 v55, 0
	v_mov_b32_e32 v54, 0
	v_mov_b32_e32 v59, 0
	v_mov_b32_e32 v58, 0
	v_mov_b32_e32 v51, 0
	v_mov_b32_e32 v50, 0
	v_mov_b32_e32 v61, 0
	v_mov_b32_e32 v60, 0
	v_mov_b32_e32 v37, 0
	v_mov_b32_e32 v36, 0
	v_mov_b32_e32 v39, 0
	v_mov_b32_e32 v38, 0
	v_mov_b32_e32 v35, 0
	v_mov_b32_e32 v34, 0
	v_mov_b32_e32 v41, 0
	v_mov_b32_e32 v40, 0
	v_mov_b32_e32 v21, 0
	v_mov_b32_e32 v20, 0
	v_mov_b32_e32 v23, 0
	v_mov_b32_e32 v22, 0
	v_mov_b32_e32 v19, 0
	v_mov_b32_e32 v18, 0
	v_mov_b32_e32 v25, 0
	v_mov_b32_e32 v24, 0
	v_mov_b32_e32 v5, 0
	v_mov_b32_e32 v4, 0
	v_mov_b32_e32 v7, 0
	v_mov_b32_e32 v6, 0
	v_mov_b32_e32 v3, 0
	v_mov_b32_e32 v2, 0
	v_mov_b32_e32 v9, 0
	v_mov_b32_e32 v8, 0
	v_mov_b32_e32 v123, 0
	v_mov_b32_e32 v122, 0
	v_mov_b32_e32 v127, 0
	v_mov_b32_e32 v126, 0
	v_mov_b32_e32 v69, 0
	v_mov_b32_e32 v68, 0
	v_mov_b32_e32 v115, 0
	v_mov_b32_e32 v114, 0
	v_mov_b32_e32 v45, 0
	v_mov_b32_e32 v44, 0
	v_mov_b32_e32 v47, 0
	v_mov_b32_e32 v46, 0
	v_mov_b32_e32 v43, 0
	v_mov_b32_e32 v42, 0
	v_mov_b32_e32 v49, 0
	v_mov_b32_e32 v48, 0
	v_mov_b32_e32 v29, 0
	v_mov_b32_e32 v28, 0
	v_mov_b32_e32 v31, 0
	v_mov_b32_e32 v30, 0
	v_mov_b32_e32 v27, 0
	v_mov_b32_e32 v26, 0
	v_mov_b32_e32 v33, 0
	v_mov_b32_e32 v32, 0
	v_mov_b32_e32 v13, 0
	v_mov_b32_e32 v12, 0
	v_mov_b32_e32 v15, 0
	v_mov_b32_e32 v14, 0
	v_mov_b32_e32 v11, 0
	v_mov_b32_e32 v10, 0
	v_mov_b32_e32 v17, 0
	v_mov_b32_e32 v16, 0
	s_branch .LBB0_1390
.Lp10_hot:
	v_mov_b32_e32 v68, v66
	v_mov_b32_e32 v69, v66
	v_cmp_lt_i32_e32 vcc, s42, v1
	s_add_u32 s55, s2, 0x100
	v_mov_b32_e32 v67, v66
	v_mov_b32_e32 v122, 0
	v_cndmask_b32_e64 v2, 0, 1, vcc
	v_mov_b64_e32 v[72:73], v[68:69]
	v_mov_b64_e32 v[76:77], v[68:69]
	v_mov_b64_e32 v[84:85], v[68:69]
	v_mov_b64_e32 v[92:93], v[68:69]
	v_mov_b64_e32 v[100:101], v[68:69]
	v_mov_b64_e32 v[108:109], v[68:69]
	v_mov_b64_e32 v[116:117], v[68:69]
	v_mov_b64_e32 v[128:129], v[68:69]
	v_mov_b64_e32 v[80:81], v[68:69]
	v_mov_b64_e32 v[88:89], v[68:69]
	v_mov_b64_e32 v[96:97], v[68:69]
	v_mov_b64_e32 v[104:105], v[68:69]
	v_mov_b64_e32 v[112:113], v[68:69]
	v_mov_b64_e32 v[120:121], v[68:69]
	v_mov_b64_e32 v[132:133], v[68:69]
	v_mov_b64_e32 v[136:137], v[68:69]
	s_addc_u32 s56, s3, 0
	s_mov_b32 s57, 0
	v_cmp_ne_u32_e64 s[2:3], 1, v2
	v_mov_b64_e32 v[70:71], v[66:67]
	v_mov_b64_e32 v[74:75], v[66:67]
	v_mov_b64_e32 v[82:83], v[66:67]
	v_mov_b64_e32 v[90:91], v[66:67]
	v_mov_b64_e32 v[98:99], v[66:67]
	v_mov_b64_e32 v[106:107], v[66:67]
	v_mov_b64_e32 v[114:115], v[66:67]
	v_mov_b64_e32 v[126:127], v[66:67]
	v_mov_b64_e32 v[78:79], v[66:67]
	v_mov_b64_e32 v[86:87], v[66:67]
	v_mov_b64_e32 v[94:95], v[66:67]
	v_mov_b64_e32 v[102:103], v[66:67]
	v_mov_b64_e32 v[110:111], v[66:67]
	v_mov_b64_e32 v[118:119], v[66:67]
	v_mov_b64_e32 v[130:131], v[66:67]
	v_mov_b64_e32 v[134:135], v[66:67]
	v_mov_b32_e32 v123, v122
	v_mov_b32_e32 v124, v122
	v_mov_b32_e32 v125, v122
	v_mov_b32_e32 v138, v122
	v_mov_b32_e32 v139, v122
	v_mov_b32_e32 v140, v122
	v_mov_b32_e32 v141, v122
	v_mov_b32_e32 v142, v122
	v_mov_b32_e32 v143, v122
	v_mov_b32_e32 v144, v122
	v_mov_b32_e32 v145, v122
	v_mov_b32_e32 v146, v122
	v_mov_b32_e32 v147, v122
	v_mov_b32_e32 v148, v122
	v_mov_b32_e32 v149, v122
	v_mov_b32_e32 v154, v122
	v_mov_b32_e32 v155, v122
	v_mov_b32_e32 v156, v122
	v_mov_b32_e32 v157, v122
	v_mov_b32_e32 v162, v122
	v_mov_b32_e32 v163, v122
	v_mov_b32_e32 v164, v122
	v_mov_b32_e32 v165, v122
	v_mov_b32_e32 v170, v122
	v_mov_b32_e32 v171, v122
	v_mov_b32_e32 v172, v122
	v_mov_b32_e32 v173, v122
	v_mov_b32_e32 v178, v122
	v_mov_b32_e32 v179, v122
	v_mov_b32_e32 v180, v122
	v_mov_b32_e32 v181, v122
	v_mov_b32_e32 v150, v122
	v_mov_b32_e32 v151, v122
	v_mov_b32_e32 v152, v122
	v_mov_b32_e32 v153, v122
	v_mov_b32_e32 v158, v122
	v_mov_b32_e32 v159, v122
	v_mov_b32_e32 v160, v122
	v_mov_b32_e32 v161, v122
	v_mov_b32_e32 v166, v122
	v_mov_b32_e32 v167, v122
	v_mov_b32_e32 v168, v122
	v_mov_b32_e32 v169, v122
	v_mov_b32_e32 v174, v122
	v_mov_b32_e32 v175, v122
	v_mov_b32_e32 v176, v122
	v_mov_b32_e32 v177, v122
	v_mov_b32_e32 v182, v122
	v_mov_b32_e32 v183, v122
	v_mov_b32_e32 v184, v122
	v_mov_b32_e32 v185, v122
	v_mov_b32_e32 v186, v122
	v_mov_b32_e32 v187, v122
	v_mov_b32_e32 v188, v122
	v_mov_b32_e32 v189, v122
	v_mov_b32_e32 v190, v122
	v_mov_b32_e32 v191, v122
	v_mov_b32_e32 v192, v122
	v_mov_b32_e32 v193, v122
	v_mov_b32_e32 v194, v122
	v_mov_b32_e32 v195, v122
	v_mov_b32_e32 v196, v122
	v_mov_b32_e32 v197, v122
	s_branch .LBB0_1385
